# P3 XB epilogue stores with sc1 (write-through)
# baseline (speedup 1.0000x reference)
.LBB0_373:
	v_mov_b32_e32 v35, v0
	s_lshl_b32 s4, s57, 8
	v_ashrrev_i32_e32 v34, 2, v35
	v_and_b32_e32 v34, 0xffffffc0, v34
	v_lshl_add_u32 v34, s56, 8, v34
	v_and_b32_e32 v36, 0xc0, v35
	v_and_or_b32 v34, v35, 15, v34
	v_lshrrev_b32_e32 v35, 1, v35
	v_and_b32_e32 v35, 24, v35
	v_or3_b32 v36, v36, s4, v35
	v_ashrrev_i32_e32 v37, 31, v36
	v_lshlrev_b64 v[174:175], 1, v[36:37]
	v_ashrrev_i32_e32 v35, 31, v34
	v_lshl_add_u64 v[36:37], s[16:17], 0, v[174:175]
	v_lshlrev_b64 v[50:51], 11, v[34:35]
	v_lshl_add_u64 v[52:53], v[36:37], 0, v[50:51]
	global_load_dwordx4 v[210:213], v[52:53], off nt
	global_load_dwordx4 v[214:217], v[52:53], off offset:64 nt
	v_or_b32_e32 v52, 16, v34
	v_ashrrev_i32_e32 v53, 31, v52
	v_lshlrev_b64 v[234:235], 11, v[52:53]
	v_lshl_add_u64 v[52:53], v[36:37], 0, v[234:235]
	global_load_dwordx4 v[218:221], v[52:53], off nt
	global_load_dwordx4 v[222:225], v[52:53], off offset:64 nt
	v_or_b32_e32 v58, 32, v34
	v_or_b32_e32 v34, 48, v34
	v_ashrrev_i32_e32 v59, 31, v58
	v_ashrrev_i32_e32 v35, 31, v34
	v_lshlrev_b64 v[186:187], 11, v[58:59]
	v_lshlrev_b64 v[184:185], 11, v[34:35]
	v_lshl_add_u64 v[182:183], v[50:51], 0, s[10:11]
	v_lshl_add_u64 v[180:181], v[50:51], 0, s[24:25]
	v_lshl_add_u64 v[178:179], v[50:51], 0, s[26:27]
	v_lshl_add_u64 v[176:177], v[50:51], 0, s[28:29]
	v_lshl_add_u64 v[34:35], s[14:15], 0, v[50:51]
	v_lshl_add_u64 v[50:51], v[36:37], 0, v[186:187]
	v_lshl_add_u64 v[52:53], v[36:37], 0, v[184:185]
	v_lshl_add_u64 v[58:59], v[36:37], 0, v[182:183]
	v_lshl_add_u64 v[60:61], v[36:37], 0, v[180:181]
	v_lshl_add_u64 v[236:237], v[36:37], 0, v[178:179]
	v_lshl_add_u64 v[36:37], v[36:37], 0, v[176:177]
	v_lshl_add_u64 v[238:239], v[34:35], 0, v[174:175]
	global_load_dwordx4 v[226:229], v[50:51], off nt
	global_load_dwordx4 v[230:233], v[50:51], off offset:64 nt
	global_load_dwordx4 v[166:169], v[52:53], off nt
	global_load_dwordx4 v[146:149], v[52:53], off offset:64 nt
	global_load_dwordx4 v[134:137], v[58:59], off nt
	global_load_dwordx4 v[122:125], v[58:59], off offset:64 nt
	global_load_dwordx4 v[110:113], v[60:61], off nt
	global_load_dwordx4 v[98:101], v[60:61], off offset:64 nt
	global_load_dwordx4 v[82:85], v[236:237], off nt
	s_nop 0
	global_load_dwordx4 v[58:61], v[236:237], off offset:64 nt
	global_load_dwordx4 v[50:53], v[36:37], off nt
	s_nop 0
	global_load_dwordx4 v[34:37], v[36:37], off offset:64 nt
	s_and_b64 vcc, exec, s[6:7]
	s_mov_b64 s[4:5], -1
	s_waitcnt vmcnt(15)
	v_lshlrev_b32_e32 v236, 16, v210
	v_and_b32_e32 v237, 0xffff0000, v210
	v_lshlrev_b32_e32 v210, 16, v211
	v_and_b32_e32 v211, 0xffff0000, v211
	v_lshlrev_b32_e32 v240, 16, v212
	v_and_b32_e32 v241, 0xffff0000, v212
	v_lshlrev_b32_e32 v212, 16, v213
	v_and_b32_e32 v213, 0xffff0000, v213
	v_pk_add_f32 v[152:153], v[152:153], v[210:211]
	v_pk_add_f32 v[150:151], v[150:151], v[236:237]
	s_waitcnt vmcnt(14)
	v_lshlrev_b32_e32 v242, 16, v214
	v_and_b32_e32 v243, 0xffff0000, v214
	v_lshlrev_b32_e32 v214, 16, v215
	v_and_b32_e32 v215, 0xffff0000, v215
	v_lshlrev_b32_e32 v244, 16, v216
	v_and_b32_e32 v245, 0xffff0000, v216
	v_lshlrev_b32_e32 v216, 16, v217
	v_and_b32_e32 v217, 0xffff0000, v217
	v_pk_add_f32 v[156:157], v[156:157], v[212:213]
	v_pk_add_f32 v[154:155], v[154:155], v[240:241]
	v_cvt_pk_bf16_f32 v150, v150, v151
	v_cvt_pk_bf16_f32 v151, v152, v153
	v_pk_add_f32 v[164:165], v[164:165], v[214:215]
	v_cvt_pk_bf16_f32 v152, v154, v155
	v_cvt_pk_bf16_f32 v153, v156, v157
	v_pk_add_f32 v[162:163], v[162:163], v[242:243]
	v_pk_add_f32 v[160:161], v[160:161], v[216:217]
	v_pk_add_f32 v[158:159], v[158:159], v[244:245]
	s_waitcnt vmcnt(13)
	v_lshlrev_b32_e32 v210, 16, v218
	v_and_b32_e32 v211, 0xffff0000, v218
	global_store_dwordx4 v[238:239], v[150:153], off sc1
	v_pk_add_f32 v[142:143], v[142:143], v[210:211]
	v_lshlrev_b32_e32 v212, 16, v219
	v_cvt_pk_bf16_f32 v150, v162, v163
	v_cvt_pk_bf16_f32 v151, v164, v165
	v_cvt_pk_bf16_f32 v152, v158, v159
	v_cvt_pk_bf16_f32 v153, v160, v161
	global_store_dwordx4 v[238:239], v[150:153], off offset:64 sc1
	v_and_b32_e32 v213, 0xffff0000, v219
	v_pk_add_f32 v[144:145], v[144:145], v[212:213]
	v_lshlrev_b32_e32 v150, 16, v220
	v_and_b32_e32 v151, 0xffff0000, v220
	v_lshlrev_b32_e32 v152, 16, v221
	v_and_b32_e32 v153, 0xffff0000, v221
	v_pk_add_f32 v[152:153], v[140:141], v[152:153]
	v_pk_add_f32 v[140:141], v[138:139], v[150:151]
	v_cvt_pk_bf16_f32 v138, v142, v143
	v_lshl_add_u64 v[142:143], s[14:15], 0, v[234:235]
	v_cvt_pk_bf16_f32 v139, v144, v145
	v_cvt_pk_bf16_f32 v140, v140, v141
	v_cvt_pk_bf16_f32 v141, v152, v153
	v_lshl_add_u64 v[142:143], v[142:143], 0, v[174:175]
	global_store_dwordx4 v[142:143], v[138:141], off sc1
	s_waitcnt vmcnt(15)
	s_nop 0
	v_lshlrev_b32_e32 v138, 16, v222
	v_and_b32_e32 v139, 0xffff0000, v222
	v_lshlrev_b32_e32 v140, 16, v223
	v_and_b32_e32 v141, 0xffff0000, v223
	v_pk_add_f32 v[132:133], v[132:133], v[140:141]
	v_pk_add_f32 v[130:131], v[130:131], v[138:139]
	v_lshlrev_b32_e32 v138, 16, v224
	v_and_b32_e32 v139, 0xffff0000, v224
	v_lshlrev_b32_e32 v140, 16, v225
	v_and_b32_e32 v141, 0xffff0000, v225
	v_pk_add_f32 v[140:141], v[128:129], v[140:141]
	v_pk_add_f32 v[128:129], v[126:127], v[138:139]
	v_cvt_pk_bf16_f32 v126, v130, v131
	v_cvt_pk_bf16_f32 v127, v132, v133
	s_nop 0
	v_cvt_pk_bf16_f32 v128, v128, v129
	v_cvt_pk_bf16_f32 v129, v140, v141
	global_store_dwordx4 v[142:143], v[126:129], off offset:64 sc1
	s_waitcnt vmcnt(15)
	s_nop 0
	v_lshlrev_b32_e32 v126, 16, v226
	v_and_b32_e32 v127, 0xffff0000, v226
	v_lshlrev_b32_e32 v128, 16, v227
	v_and_b32_e32 v129, 0xffff0000, v227
	v_pk_add_f32 v[120:121], v[120:121], v[128:129]
	v_pk_add_f32 v[118:119], v[118:119], v[126:127]
	v_lshlrev_b32_e32 v126, 16, v228
	v_and_b32_e32 v127, 0xffff0000, v228
	v_lshlrev_b32_e32 v128, 16, v229
	v_and_b32_e32 v129, 0xffff0000, v229
	v_pk_add_f32 v[128:129], v[116:117], v[128:129]
	v_pk_add_f32 v[116:117], v[114:115], v[126:127]
	v_cvt_pk_bf16_f32 v114, v118, v119
	v_lshl_add_u64 v[118:119], s[14:15], 0, v[186:187]
	v_cvt_pk_bf16_f32 v115, v120, v121
	v_cvt_pk_bf16_f32 v116, v116, v117
	v_cvt_pk_bf16_f32 v117, v128, v129
	v_lshl_add_u64 v[118:119], v[118:119], 0, v[174:175]
	global_store_dwordx4 v[118:119], v[114:117], off sc1
	s_waitcnt vmcnt(15)
	s_nop 0
	v_lshlrev_b32_e32 v114, 16, v230
	v_and_b32_e32 v115, 0xffff0000, v230
	v_lshlrev_b32_e32 v116, 16, v231
	v_and_b32_e32 v117, 0xffff0000, v231
	v_pk_add_f32 v[108:109], v[108:109], v[116:117]
	v_pk_add_f32 v[106:107], v[106:107], v[114:115]
	v_lshlrev_b32_e32 v114, 16, v232
	v_and_b32_e32 v115, 0xffff0000, v232
	v_lshlrev_b32_e32 v116, 16, v233
	v_and_b32_e32 v117, 0xffff0000, v233
	v_pk_add_f32 v[116:117], v[104:105], v[116:117]
	v_pk_add_f32 v[104:105], v[102:103], v[114:115]
	v_cvt_pk_bf16_f32 v102, v106, v107
	v_cvt_pk_bf16_f32 v103, v108, v109
	s_nop 0
	v_cvt_pk_bf16_f32 v104, v104, v105
	v_cvt_pk_bf16_f32 v105, v116, v117
	global_store_dwordx4 v[118:119], v[102:105], off offset:64 sc1
	s_waitcnt vmcnt(15)
	s_nop 0
	v_lshlrev_b32_e32 v102, 16, v166
	v_and_b32_e32 v103, 0xffff0000, v166
	v_lshlrev_b32_e32 v104, 16, v167
	v_and_b32_e32 v105, 0xffff0000, v167
	v_pk_add_f32 v[96:97], v[96:97], v[104:105]
	v_pk_add_f32 v[94:95], v[94:95], v[102:103]
	v_lshlrev_b32_e32 v102, 16, v168
	v_and_b32_e32 v103, 0xffff0000, v168
	v_lshlrev_b32_e32 v104, 16, v169
	v_and_b32_e32 v105, 0xffff0000, v169
	v_pk_add_f32 v[104:105], v[92:93], v[104:105]
	v_pk_add_f32 v[92:93], v[90:91], v[102:103]
	v_cvt_pk_bf16_f32 v90, v94, v95
	v_lshl_add_u64 v[94:95], s[14:15], 0, v[184:185]
	v_cvt_pk_bf16_f32 v91, v96, v97
	v_cvt_pk_bf16_f32 v92, v92, v93
	v_cvt_pk_bf16_f32 v93, v104, v105
	v_lshl_add_u64 v[94:95], v[94:95], 0, v[174:175]
	global_store_dwordx4 v[94:95], v[90:93], off sc1
	s_waitcnt vmcnt(15)
	s_nop 0
	v_lshlrev_b32_e32 v90, 16, v146
	v_and_b32_e32 v91, 0xffff0000, v146
	v_lshlrev_b32_e32 v92, 16, v147
	v_and_b32_e32 v93, 0xffff0000, v147
	v_pk_add_f32 v[80:81], v[80:81], v[92:93]
	v_pk_add_f32 v[78:79], v[78:79], v[90:91]
	v_lshlrev_b32_e32 v90, 16, v148
	v_and_b32_e32 v91, 0xffff0000, v148
	v_lshlrev_b32_e32 v92, 16, v149
	v_and_b32_e32 v93, 0xffff0000, v149
	v_pk_add_f32 v[92:93], v[72:73], v[92:93]
	v_pk_add_f32 v[72:73], v[70:71], v[90:91]
	v_cvt_pk_bf16_f32 v70, v78, v79
	v_cvt_pk_bf16_f32 v71, v80, v81
	s_waitcnt vmcnt(14)
	v_lshlrev_b32_e32 v78, 16, v136
	v_cvt_pk_bf16_f32 v72, v72, v73
	v_cvt_pk_bf16_f32 v73, v92, v93
	global_store_dwordx4 v[94:95], v[70:73], off offset:64 sc1
	v_and_b32_e32 v79, 0xffff0000, v136
	v_pk_add_f32 v[74:75], v[74:75], v[78:79]
	v_lshlrev_b32_e32 v70, 16, v134
	v_and_b32_e32 v71, 0xffff0000, v134
	v_lshlrev_b32_e32 v72, 16, v135
	v_and_b32_e32 v73, 0xffff0000, v135
	v_pk_add_f32 v[72:73], v[88:89], v[72:73]
	v_pk_add_f32 v[70:71], v[86:87], v[70:71]
	v_lshlrev_b32_e32 v80, 16, v137
	v_and_b32_e32 v81, 0xffff0000, v137
	v_cvt_pk_bf16_f32 v70, v70, v71
	v_cvt_pk_bf16_f32 v71, v72, v73
	v_cvt_pk_bf16_f32 v72, v74, v75
	v_lshl_add_u64 v[74:75], s[14:15], 0, v[182:183]
	v_pk_add_f32 v[76:77], v[76:77], v[80:81]
	v_lshl_add_u64 v[74:75], v[74:75], 0, v[174:175]
	v_cvt_pk_bf16_f32 v73, v76, v77
	global_store_dwordx4 v[74:75], v[70:73], off sc1
	s_waitcnt vmcnt(15)
	s_nop 0
	v_lshlrev_b32_e32 v70, 16, v122
	v_and_b32_e32 v71, 0xffff0000, v122
	v_lshlrev_b32_e32 v72, 16, v123
	v_and_b32_e32 v73, 0xffff0000, v123
	v_pk_add_f32 v[68:69], v[68:69], v[72:73]
	v_pk_add_f32 v[66:67], v[66:67], v[70:71]
	v_lshlrev_b32_e32 v70, 16, v124
	v_and_b32_e32 v71, 0xffff0000, v124
	v_lshlrev_b32_e32 v72, 16, v125
	v_and_b32_e32 v73, 0xffff0000, v125
	v_pk_add_f32 v[72:73], v[64:65], v[72:73]
	v_pk_add_f32 v[64:65], v[62:63], v[70:71]
	v_cvt_pk_bf16_f32 v62, v66, v67
	v_cvt_pk_bf16_f32 v63, v68, v69
	s_nop 0
	v_cvt_pk_bf16_f32 v64, v64, v65
	v_cvt_pk_bf16_f32 v65, v72, v73
	global_store_dwordx4 v[74:75], v[62:65], off offset:64 sc1
	s_waitcnt vmcnt(15)
	s_nop 0
	v_lshlrev_b32_e32 v62, 16, v110
	v_and_b32_e32 v63, 0xffff0000, v110
	v_lshlrev_b32_e32 v64, 16, v111
	v_and_b32_e32 v65, 0xffff0000, v111
	v_pk_add_f32 v[56:57], v[56:57], v[64:65]
	v_pk_add_f32 v[54:55], v[54:55], v[62:63]
	v_lshlrev_b32_e32 v62, 16, v112
	v_and_b32_e32 v63, 0xffff0000, v112
	v_lshlrev_b32_e32 v64, 16, v113
	v_and_b32_e32 v65, 0xffff0000, v113
	v_pk_add_f32 v[64:65], v[48:49], v[64:65]
	v_pk_add_f32 v[48:49], v[46:47], v[62:63]
	v_cvt_pk_bf16_f32 v46, v54, v55
	v_lshl_add_u64 v[54:55], s[14:15], 0, v[180:181]
	v_cvt_pk_bf16_f32 v47, v56, v57
	v_cvt_pk_bf16_f32 v48, v48, v49
	v_cvt_pk_bf16_f32 v49, v64, v65
	v_lshl_add_u64 v[54:55], v[54:55], 0, v[174:175]
	global_store_dwordx4 v[54:55], v[46:49], off sc1
	s_waitcnt vmcnt(15)
	s_nop 0
	v_lshlrev_b32_e32 v46, 16, v98
	v_and_b32_e32 v47, 0xffff0000, v98
	v_lshlrev_b32_e32 v48, 16, v99
	v_and_b32_e32 v49, 0xffff0000, v99
	v_pk_add_f32 v[44:45], v[44:45], v[48:49]
	v_pk_add_f32 v[42:43], v[42:43], v[46:47]
	v_lshlrev_b32_e32 v46, 16, v100
	v_and_b32_e32 v47, 0xffff0000, v100
	v_lshlrev_b32_e32 v48, 16, v101
	v_and_b32_e32 v49, 0xffff0000, v101
	v_pk_add_f32 v[48:49], v[40:41], v[48:49]
	v_pk_add_f32 v[40:41], v[38:39], v[46:47]
	v_cvt_pk_bf16_f32 v38, v42, v43
	v_cvt_pk_bf16_f32 v39, v44, v45
	s_nop 0
	v_cvt_pk_bf16_f32 v40, v40, v41
	v_cvt_pk_bf16_f32 v41, v48, v49
	global_store_dwordx4 v[54:55], v[38:41], off offset:64 sc1
	s_waitcnt vmcnt(15)
	s_nop 0
	v_lshlrev_b32_e32 v38, 16, v82
	v_and_b32_e32 v39, 0xffff0000, v82
	v_lshlrev_b32_e32 v40, 16, v83
	v_and_b32_e32 v41, 0xffff0000, v83
	v_pk_add_f32 v[32:33], v[32:33], v[40:41]
	v_pk_add_f32 v[30:31], v[30:31], v[38:39]
	v_lshlrev_b32_e32 v38, 16, v84
	v_and_b32_e32 v39, 0xffff0000, v84
	v_lshlrev_b32_e32 v40, 16, v85
	v_and_b32_e32 v41, 0xffff0000, v85
	v_pk_add_f32 v[40:41], v[28:29], v[40:41]
	v_pk_add_f32 v[28:29], v[26:27], v[38:39]
	v_cvt_pk_bf16_f32 v26, v30, v31
	v_lshl_add_u64 v[30:31], s[14:15], 0, v[178:179]
	v_cvt_pk_bf16_f32 v27, v32, v33
	v_cvt_pk_bf16_f32 v28, v28, v29
	v_cvt_pk_bf16_f32 v29, v40, v41
	v_lshl_add_u64 v[30:31], v[30:31], 0, v[174:175]
	global_store_dwordx4 v[30:31], v[26:29], off sc1
	s_waitcnt vmcnt(15)
	s_nop 0
	v_lshlrev_b32_e32 v26, 16, v58
	v_and_b32_e32 v27, 0xffff0000, v58
	v_lshlrev_b32_e32 v28, 16, v59
	v_and_b32_e32 v29, 0xffff0000, v59
	v_pk_add_f32 v[24:25], v[24:25], v[28:29]
	v_pk_add_f32 v[22:23], v[22:23], v[26:27]
	v_lshlrev_b32_e32 v26, 16, v60
	v_and_b32_e32 v27, 0xffff0000, v60
	v_lshlrev_b32_e32 v28, 16, v61
	v_and_b32_e32 v29, 0xffff0000, v61
	v_pk_add_f32 v[28:29], v[20:21], v[28:29]
	v_pk_add_f32 v[20:21], v[18:19], v[26:27]
	v_cvt_pk_bf16_f32 v18, v22, v23
	v_cvt_pk_bf16_f32 v19, v24, v25
	s_nop 0
	v_cvt_pk_bf16_f32 v20, v20, v21
	v_cvt_pk_bf16_f32 v21, v28, v29
	global_store_dwordx4 v[30:31], v[18:21], off offset:64 sc1
	s_waitcnt vmcnt(15)
	s_nop 0
	v_lshlrev_b32_e32 v18, 16, v50
	v_and_b32_e32 v19, 0xffff0000, v50
	v_lshlrev_b32_e32 v20, 16, v51
	v_and_b32_e32 v21, 0xffff0000, v51
	v_pk_add_f32 v[16:17], v[16:17], v[20:21]
	v_pk_add_f32 v[14:15], v[14:15], v[18:19]
	v_lshlrev_b32_e32 v18, 16, v52
	v_and_b32_e32 v19, 0xffff0000, v52
	v_lshlrev_b32_e32 v20, 16, v53
	v_and_b32_e32 v21, 0xffff0000, v53
	v_pk_add_f32 v[20:21], v[12:13], v[20:21]
	v_pk_add_f32 v[12:13], v[10:11], v[18:19]
	v_cvt_pk_bf16_f32 v10, v14, v15
	v_lshl_add_u64 v[14:15], s[14:15], 0, v[176:177]
	v_cvt_pk_bf16_f32 v11, v16, v17
	v_cvt_pk_bf16_f32 v12, v12, v13
	v_cvt_pk_bf16_f32 v13, v20, v21
	v_lshl_add_u64 v[14:15], v[14:15], 0, v[174:175]
	global_store_dwordx4 v[14:15], v[10:13], off sc1
	s_waitcnt vmcnt(15)
	s_nop 0
	v_lshlrev_b32_e32 v10, 16, v34
	v_and_b32_e32 v11, 0xffff0000, v34
	v_lshlrev_b32_e32 v12, 16, v35
	v_and_b32_e32 v13, 0xffff0000, v35
	v_pk_add_f32 v[8:9], v[8:9], v[12:13]
	v_pk_add_f32 v[6:7], v[6:7], v[10:11]
	v_lshlrev_b32_e32 v10, 16, v36
	v_and_b32_e32 v11, 0xffff0000, v36
	v_lshlrev_b32_e32 v12, 16, v37
	v_and_b32_e32 v13, 0xffff0000, v37
	v_pk_add_f32 v[12:13], v[4:5], v[12:13]
	v_pk_add_f32 v[4:5], v[2:3], v[10:11]
	v_cvt_pk_bf16_f32 v2, v6, v7
	v_cvt_pk_bf16_f32 v3, v8, v9
	s_nop 0
	v_cvt_pk_bf16_f32 v4, v4, v5
	v_cvt_pk_bf16_f32 v5, v12, v13
	global_store_dwordx4 v[14:15], v[2:5], off offset:64 sc1
	s_cbranch_vccnz .LBB0_360
	s_andn2_b64 vcc, exec, s[12:13]
	s_cbranch_vccnz .LBB0_359
	s_barrier
	s_branch .LBB0_359
